# GLA pass B: gate-weight loads and state-fold loop de-serialised (all loads of a fold step issued then one wait); diff loop: fragment address arithmetic hoisted
# speedup vs baseline: 1.0138x; 1.0138x over previous
; template <int KW, int DV, bool MASK> ...
;     constexpr int KRB = KW * 2, KB = 64 * KRB, VB = DV * 128, SLOT = KB + VB, NKC = KB / 8192, NVC = VB / 8192, NDMA = NKC + NVC;
;     const int r32 = F.lane & 31, hi = F.lane >> 5, nt = nctx + nloc;
;     ...
;     f32x16 s0, s1; bf16x8 pa[4];
;     ...
;     unsigned kad[4], vad[4];
; #pragma unroll
;     for (int i = 0; i < 4; ++i) { const int c = 2 * i + hi;
;         kad[i] = (unsigned)(uintptr_t)F.lds + (KW == 128 ? r32 * 256 + ((((koff >> 3) + c) ^ (r32 & 15)) << 4) : r32 * 128 + ((c ^ ((r32 >> 1) & 7)) << 4));
;         vad[i] = (unsigned)(uintptr_t)F.lds + KB + r32 * 128 + ((c ^ ((r32 >> 1) & 7)) << 4); }
;     __syncthreads();
;     ATT_DMA(0);
;     if (nt > 1) ATT_DMA(1);
; __device__ __forceinline__ float score_bound(const float* wq, const float* wk, int lane) {
;     float a = fabsf(wq[lane]), c = fabsf(wk[lane]);
; #pragma unroll
;     for (int o = 1; o < 64; o <<= 1) { a = fmaxf(a, __shfl_xor(a, o)); c = fmaxf(c, __shfl_xor(c, o)); }
;     return 64.f * a * c * 0.125f * LOG2E;
; }
; __device__ __forceinline__ void diff_unit(KP Pk, Frame& F, int l, int b, int h, int qrow0, int nkt) {
;     unsigned char* ws = F.ws;
;     const bf16_t* U = (const bf16_t*)(ws + WS_U);
;     const int m = F.wave & 1, rb = F.wave >> 1;
;     const float sh2 = score_bound(Pk->in[I_DQN] + l * 64, Pk->in[I_DKN] + l * 64, F.lane);
;     bf16x8 q[4];
;     { const bf16_t* qp = U + (size_t)(qrow0 + 32 * rb + (F.lane & 31)) * NU + UC_DQ + h * 128 + m * 64 + 8 * (F.lane >> 5);
; #pragma unroll
;       for (int ks = 0; ks < 4; ++ks) q[ks] = *(const bf16x8*)(qp + 16 * ks); }
;     f32x16 O[4];
; #pragma unroll
;     for (int nb = 0; nb < 4; ++nb) O[nb] = (f32x16){};
;     float lsum = 0.f;
;     attn_core<128, 128, false>(F, U, b, UC_DK + h * 128, (const bf16_t*)(ws + WS_VTD) + ((size_t)(b * 4 + h) * 128) * KEYS, nkt, 0, 0, q, 64 * m, 0, sh2, O, lsum);
.LBB0_625:
	s_andn2_b64 vcc, exec, s[8:9]
	s_cbranch_vccnz .LBB0_639
	v_readlane_b32 s5, v255, 26
	s_ashr_i32 s4, s5, 31
	s_lshr_b32 s4, s4, 23
	s_add_i32 s4, s5, s4
	s_and_b32 s4, s4, 0xfffffe00
	s_load_dwordx4 s[40:43], s[48:49], 0xc8
	s_sub_i32 s4, s5, s4
	s_ashr_i32 s34, s4, 6
	s_bfe_u32 s35, s4, 0x20004
	s_lshl_b32 s4, s4, 7
	s_lshl_b32 s19, s34, 11
	s_and_b32 s4, s4, 0x780
	s_or_b32 s18, s19, s4
	s_waitcnt lgkmcnt(0)
	s_add_u32 s4, s40, s52
	s_addc_u32 s5, s41, s53
	v_ashrrev_i32_e32 v177, 31, v176
	s_add_u32 s8, s42, s52
	v_lshlrev_b64 v[2:3], 2, v[176:177]
	s_addc_u32 s9, s43, s53
	v_lshl_add_u64 v[4:5], s[4:5], 0, v[2:3]
	global_load_dword v6, v[4:5], off
	v_lshl_add_u64 v[2:3], s[8:9], 0, v[2:3]
	global_load_dword v7, v[2:3], off
	v_cmp_lt_i32_e32 vcc, v232, v234
	v_xor_b32_e32 v1, 1, v231
	v_xor_b32_e32 v4, 2, v231
	v_cndmask_b32_e32 v9, v231, v232, vcc
	v_cmp_lt_i32_e32 vcc, v235, v234
	v_xor_b32_e32 v5, 4, v231
	v_xor_b32_e32 v8, 8, v231
	v_cndmask_b32_e32 v10, v231, v235, vcc
	v_cmp_lt_i32_e32 vcc, v1, v234
	v_ashrrev_i32_e32 v12, 5, v176
	v_lshlrev_b32_e32 v13, 8, v176
	v_cndmask_b32_e32 v14, v231, v1, vcc
	v_cmp_lt_i32_e32 vcc, v4, v234
	v_ashrrev_i32_e32 v11, 2, v176
	v_lshlrev_b32_e32 v1, 2, v9
	v_cndmask_b32_e32 v15, v231, v4, vcc
	v_cmp_lt_i32_e32 vcc, v5, v234
	v_lshlrev_b32_e32 v143, 2, v10
	v_and_b32_e32 v9, 0x1f00, v13
	v_cndmask_b32_e32 v5, v231, v5, vcc
	v_cmp_lt_i32_e32 vcc, v8, v234
	v_add_u32_e32 v10, s36, v12
	v_and_b32_e32 v4, -8, v11
	v_cndmask_b32_e32 v8, v231, v8, vcc
	v_lshlrev_b32_e32 v139, 2, v8
	v_add_u32_e32 v8, 0, v9
	v_bitop3_b32 v9, v10, v176, 15 bitop3:0x78
	v_add_u32_e32 v11, 2, v10
	v_add_u32_e32 v12, 4, v10
	v_add_u32_e32 v10, 6, v10
	v_readlane_b32 s4, v253, 13
	v_lshl_add_u32 v13, v9, 4, v8
	v_bitop3_b32 v9, v11, v176, 15 bitop3:0x78
	v_bitop3_b32 v11, v12, v176, 15 bitop3:0x78
	v_bitop3_b32 v10, v10, v176, 15 bitop3:0x78
	s_add_i32 s40, s18, s4
	v_mov_b64_e32 v[2:3], s[56:57]
	v_lshl_add_u32 v12, v9, 4, v8
	v_lshl_add_u32 v11, v11, 4, v8
	v_lshl_add_u32 v10, v10, 4, v8
	s_lshl_b32 s8, s34, 2
	v_and_or_b32 v8, v176, 31, s40
	s_lshl_b32 s60, s35, 8
	v_readlane_b32 s4, v253, 15
	s_or_b32 s26, s8, s35
	v_mad_i64_i32 v[2:3], s[8:9], v8, s30, v[2:3]
	s_mov_b32 s5, s61
	s_lshl_b32 s4, s4, 1
	v_lshl_add_u64 v[2:3], v[2:3], 0, s[60:61]
	v_lshlrev_b32_e32 v140, 2, v5
	v_ashrrev_i32_e32 v5, 31, v4
	v_lshl_add_u64 v[2:3], v[2:3], 0, s[4:5]
	v_lshlrev_b32_e32 v142, 2, v14
	v_lshl_add_u64 v[2:3], v[4:5], 1, v[2:3]
	v_lshlrev_b32_e32 v141, 2, v15
	s_mul_i32 s26, s26, 0x90000
	s_lshl_b32 s18, s35, 7
	s_ashr_i32 s8, s26, 31
	v_readlane_b32 s4, v254, 59
	s_add_u32 s26, s4, s26
	v_readlane_b32 s4, v254, 60
	s_addc_u32 s27, s4, s8
	s_mov_b64 s[4:5], 0x1e00
	v_readlane_b32 s38, v253, 16
	v_readlane_b32 s44, v253, 21
	v_mov_b32_e32 v63, v0
	s_mov_b32 m0, s44
	v_mov_b32_e32 v65, v0
	v_ashrrev_i32_e32 v16, 3, v176
	v_add_u32_e32 v82, s21, v16
	v_lshrrev_b32_e32 v83, 1, v82
	s_movk_i32 s41, 0xc0
	s_mul_i32 s35, s35, 0x90000
	v_mov_b32_e32 v144, 0
	s_waitcnt vmcnt(1)
	v_and_b32_e32 v4, 0x7fffffff, v6
	ds_bpermute_b32 v4, v142, v4
	s_waitcnt vmcnt(0)
	v_and_b32_e32 v5, 0x7fffffff, v7
	ds_bpermute_b32 v5, v142, v5
	v_max_f32_e64 v6, |v6|, |v6|
	v_max_f32_e64 v7, |v7|, |v7|
	s_waitcnt lgkmcnt(1)
	v_max_f32_e32 v4, v4, v4
	v_max_f32_e32 v6, v6, v4
	s_waitcnt lgkmcnt(0)
	v_max_f32_e32 v4, v5, v5
	ds_bpermute_b32 v8, v141, v6
	v_max_f32_e32 v7, v7, v4
	ds_bpermute_b32 v9, v141, v7
	v_lshl_add_u64 v[4:5], v[2:3], 0, s[4:5]
	v_add_co_u32_e32 v2, vcc, s1, v2
	s_waitcnt lgkmcnt(1)
	v_max_f32_e32 v8, v8, v8
	v_max_f32_e32 v6, v6, v8
	s_waitcnt lgkmcnt(0)
	v_max_f32_e32 v8, v9, v9
	ds_bpermute_b32 v9, v140, v6
	v_max_f32_e32 v7, v7, v8
	ds_bpermute_b32 v8, v140, v7
	v_addc_co_u32_e32 v3, vcc, 0, v3, vcc
	s_waitcnt lgkmcnt(1)
	v_max_f32_e32 v9, v9, v9
	v_max_f32_e32 v6, v6, v9
	s_waitcnt lgkmcnt(0)
	v_max_f32_e32 v8, v8, v8
	ds_bpermute_b32 v9, v139, v6
	v_max_f32_e32 v7, v7, v8
	ds_bpermute_b32 v8, v139, v7
	global_load_dwordx4 v[114:117], v[4:5], off offset:32
	global_load_dwordx4 v[118:121], v[4:5], off offset:64
	global_load_dwordx4 v[122:125], v[2:3], off offset:3584
	global_load_dwordx4 v[126:129], v[4:5], off offset:96
	s_waitcnt lgkmcnt(1)
	v_max_f32_e32 v9, v9, v9
	v_max_f32_e32 v6, v6, v9
	s_waitcnt lgkmcnt(0)
	v_max_f32_e32 v8, v8, v8
	ds_bpermute_b32 v9, v1, v6
	v_max_f32_e32 v7, v7, v8
	ds_bpermute_b32 v8, v1, v7
	s_add_u32 s4, s56, s60
	s_addc_u32 s5, s57, 0
	s_waitcnt lgkmcnt(1)
	v_max_f32_e32 v2, v9, v9
	v_max_f32_e32 v2, v6, v2
	s_waitcnt lgkmcnt(0)
	v_max_f32_e32 v3, v8, v8
	ds_bpermute_b32 v4, v143, v2
	v_max_f32_e32 v3, v7, v3
	ds_bpermute_b32 v5, v143, v3
	s_add_u32 s8, s4, 0x2200
	s_addc_u32 s9, s5, 0
	s_waitcnt lgkmcnt(1)
	v_max_f32_e32 v4, v4, v4
	v_max_f32_e32 v2, v2, v4
	s_waitcnt lgkmcnt(0)
	v_max_f32_e32 v4, v5, v5
	s_lshl_b32 s37, s34, 8
	v_ashrrev_i32_e32 v6, 4, v176
	v_mul_f32_e32 v2, 0x42800000, v2
	v_max_f32_e32 v3, v3, v4
	s_add_i32 s4, s19, 0xffffff00
	s_add_i32 s5, s37, 0x4000
	v_add_u32_e32 v138, s38, v6
	v_mul_f32_e32 v2, v2, v3
	v_mov_b32_e32 v8, s4
	v_mov_b32_e32 v9, s5
	v_cmp_gt_i32_e32 vcc, s70, v138
	v_mul_f32_e32 v14, 0x3e000000, v2
	v_xor_b32_e32 v7, v138, v176
	v_cndmask_b32_e32 v2, v8, v9, vcc
	v_add_u32_e32 v4, v2, v138
	v_mov_b64_e32 v[2:3], s[8:9]
	v_mad_i64_i32 v[4:5], s[38:39], v4, s30, v[2:3]
	v_lshlrev_b32_e32 v7, 4, v7
	v_readlane_b32 s38, v253, 10
	v_and_b32_e32 v62, 0xf0, v7
	v_lshl_add_u64 v[4:5], v[4:5], 0, v[62:63]
	v_add_u32_e32 v15, s38, v6
	v_cmp_gt_i32_e32 vcc, s70, v15
	s_barrier
; template <int KW, int DV, bool MASK> ...
;     ...
;     f32x16 s0, s1; bf16x8 pa[4];
;     ...
;     unsigned kad[4], vad[4];
; #pragma unroll
;     for (int i = 0; i < 4; ++i) { const int c = 2 * i + hi;
;         kad[i] = (unsigned)(uintptr_t)F.lds + (KW == 128 ? r32 * 256 + ((((koff >> 3) + c) ^ (r32 & 15)) << 4) : r32 * 128 + ((c ^ ((r32 >> 1) & 7)) << 4));
;         vad[i] = (unsigned)(uintptr_t)F.lds + KB + r32 * 128 + ((c ^ ((r32 >> 1) & 7)) << 4); }
;     __syncthreads();
;     ATT_DMA(0);
;     if (nt > 1) ATT_DMA(1);
;     if (nt > 2) ATT_DMA(2);
;     if (nt > 2) asm volatile("s_waitcnt vmcnt(%0)" :: "n"(NDMA) : "memory"); else asm volatile("s_waitcnt vmcnt(0)" ::: "memory");
;     __syncthreads();
	global_load_lds_dwordx4 v[4:5], off
	v_cndmask_b32_e32 v4, v8, v9, vcc
	v_add_u32_e32 v4, v4, v15
	v_xor_b32_e32 v6, v15, v176
	v_mad_i64_i32 v[4:5], s[38:39], v4, s30, v[2:3]
	v_lshlrev_b32_e32 v6, 4, v6
	v_readlane_b32 s39, v253, 11
	v_and_b32_e32 v64, 0xf0, v6
	s_add_i32 s38, s39, 0
	v_lshl_add_u64 v[4:5], v[4:5], 0, v[64:65]
	s_mov_b32 m0, s38
	v_xor_b32_e32 v8, v83, v176
	global_load_lds_dwordx4 v[4:5], off
	v_mov_b64_e32 v[4:5], s[26:27]
	v_mad_i64_i32 v[6:7], s[26:27], v82, s64, v[4:5]
	v_readlane_b32 s26, v253, 12
	v_lshlrev_b32_e32 v8, 4, v8
	v_and_b32_e32 v8, 0x70, v8
	v_add_u32_e32 v84, s26, v16
	v_mov_b32_e32 v9, v0
	v_lshrrev_b32_e32 v85, 1, v84
	v_lshl_add_u64 v[6:7], v[6:7], 0, v[8:9]
	v_xor_b32_e32 v8, v85, v176
	v_mad_i64_i32 v[4:5], s[26:27], v84, s64, v[4:5]
	v_lshlrev_b32_e32 v8, 4, v8
	s_add_i32 s26, s19, 0xffffff40
	s_add_i32 s27, s37, 0x4040
	v_and_b32_e32 v8, 0x70, v8
	v_mov_b32_e32 v16, s26
	v_mov_b32_e32 v17, s27
	v_cmp_gt_i32_e32 vcc, s41, v138
	v_lshl_add_u64 v[4:5], v[4:5], 0, v[8:9]
	s_add_i32 m0, s44, 0x4000
	v_cndmask_b32_e32 v8, v16, v17, vcc
	v_add_u32_e32 v8, v8, v138
	global_load_lds_dwordx4 v[6:7], off
	s_add_i32 m0, s38, 0x4000
	v_mad_i64_i32 v[8:9], s[26:27], v8, s30, v[2:3]
	global_load_lds_dwordx4 v[4:5], off
	v_lshl_add_u64 v[8:9], v[8:9], 0, v[62:63]
	s_add_i32 m0, s44, 0x8000
	v_cmp_gt_i32_e32 vcc, s41, v15
	global_load_lds_dwordx4 v[8:9], off
	s_nop 0
	v_cndmask_b32_e32 v8, v16, v17, vcc
	v_add_u32_e32 v8, v8, v15
	v_mad_i64_i32 v[8:9], s[26:27], v8, s30, v[2:3]
	v_lshl_add_u64 v[8:9], v[8:9], 0, v[64:65]
	s_add_i32 m0, s38, 0x8000
	s_addk_i32 s19, 0xff80
	global_load_lds_dwordx4 v[8:9], off
	v_lshl_add_u64 v[8:9], v[6:7], 0, s[24:25]
	s_add_i32 m0, s44, 0xc000
	s_add_i32 s26, s37, 0x4080
	global_load_lds_dwordx4 v[8:9], off
	s_add_i32 m0, s38, 0xc000
	s_movk_i32 s38, 0x80
	v_lshl_add_u64 v[8:9], v[4:5], 0, s[24:25]
	v_mov_b32_e32 v16, s19
	v_mov_b32_e32 v17, s26
	v_cmp_gt_i32_e32 vcc, s38, v138
	global_load_lds_dwordx4 v[8:9], off
	s_nop 0
	v_cndmask_b32_e32 v8, v16, v17, vcc
	v_add_u32_e32 v8, v8, v138
	v_mad_i64_i32 v[8:9], s[26:27], v8, s30, v[2:3]
	s_add_i32 s19, 0, 0x10000
	v_readlane_b32 s37, v253, 55
	v_lshl_add_u64 v[8:9], v[8:9], 0, v[62:63]
	s_add_i32 m0, s19, s37
	v_cmp_gt_i32_e32 vcc, s38, v15
	global_load_lds_dwordx4 v[8:9], off
	s_nop 0
	v_cndmask_b32_e32 v8, v16, v17, vcc
	v_add_u32_e32 v8, v8, v15
	v_mad_i64_i32 v[2:3], s[26:27], v8, s30, v[2:3]
	v_lshl_add_u64 v[2:3], v[2:3], 0, v[64:65]
	s_add_i32 m0, s19, s39
	s_mov_b64 s[26:27], 0x100
	s_add_i32 s19, 0, 0x14000
	global_load_lds_dwordx4 v[2:3], off
	v_lshl_add_u64 v[2:3], v[6:7], 0, s[26:27]
	s_add_i32 m0, s19, s37
	v_mul_f32_e32 v66, 0xbfb8aa3b, v14
	global_load_lds_dwordx4 v[2:3], off
	v_lshl_add_u64 v[2:3], v[4:5], 0, s[26:27]
	s_add_i32 m0, s19, s39
	v_mov_b32_e32 v67, v66
	global_load_lds_dwordx4 v[2:3], off
	s_waitcnt vmcnt(4)
	s_waitcnt vmcnt(0) lgkmcnt(0)
	s_barrier
; #define MFMA32(a, b, c) __builtin_amdgcn_mfma_f32_32x32x16_bf16((a), (b), (c), 0, 0, 0)
; #define LWAIT4(f) asm volatile("s_waitcnt lgkmcnt(0)" : "+v"(f[0]), "+v"(f[1]), "+v"(f[2]), "+v"(f[3]))
; #define RD_K(f, h) do { DSR(f[0], ka[2 * (h)], 0); DSR(f[1], ka[2 * (h)], 32 * KRB); DSR(f[2], ka[2 * (h) + 1], 0); DSR(f[3], ka[2 * (h) + 1], 32 * KRB); } while (0)
; template <int KW, int DV, bool MASK> ...
;     ...
;     {
;         bf16x8 fa[4], fb[4]; unsigned ka[4];
; #pragma unroll
;         for (int i = 0; i < 4; ++i) ka[i] = kad[i];
;         RD_K(fa, 0); RD_K(fb, 1);
; #pragma unroll
;         for (int r = 0; r < 16; ++r) { s0[r] = -sh2; s1[r] = -sh2; }
;         LWAIT4(fa); LWAIT4(fb);
;         s0 = MFMA32(fa[0], q[0], s0); s1 = MFMA32(fa[1], q[0], s1); s0 = MFMA32(fa[2], q[1], s0); s1 = MFMA32(fa[3], q[1], s1);
;         s0 = MFMA32(fb[0], q[2], s0); s1 = MFMA32(fb[1], q[2], s1); s0 = MFMA32(fb[2], q[3], s0); s1 = MFMA32(fb[3], q[3], s1);
; #pragma unroll
;         for (int r = 0; r < 16; ++r) EXP1(0, r);
;     }
	ds_read_b128 v[18:21], v13 offset:0
	ds_read_b128 v[34:37], v13 offset:0x2000
	ds_read_b128 v[38:41], v12 offset:0
	ds_read_b128 v[42:45], v12 offset:0x2000
	ds_read_b128 v[46:49], v11 offset:0
	ds_read_b128 v[50:53], v11 offset:0x2000
	ds_read_b128 v[54:57], v10 offset:0
	ds_read_b128 v[58:61], v10 offset:0x2000
	v_mov_b32_e32 v68, v66
	v_mov_b32_e32 v69, v66
	v_mov_b32_e32 v70, v66
	v_mov_b32_e32 v71, v66
	v_mov_b32_e32 v72, v66
	v_mov_b32_e32 v73, v66
	v_mov_b32_e32 v74, v66
	v_mov_b32_e32 v75, v66
	v_mov_b32_e32 v76, v66
	v_mov_b32_e32 v77, v66
	v_mov_b32_e32 v78, v66
	v_mov_b32_e32 v79, v66
	v_mov_b32_e32 v80, v66
	v_mov_b32_e32 v81, v66
	s_waitcnt lgkmcnt(0)
	s_waitcnt lgkmcnt(0)
	v_lshl_add_u64 v[130:131], s[8:9], 0, v[62:63]
	v_lshl_add_u64 v[132:133], s[8:9], 0, v[64:65]
	v_mfma_f32_32x32x16_bf16 v[2:17], v[18:21], v[122:125], v[66:81]
	s_mul_i32 s8, s34, 0x240000
	s_add_i32 s8, s8, s35
	s_ashr_i32 s9, s8, 31
	s_mov_b32 s19, 0
	s_mov_b32 s34, 0x18000
	s_mov_b32 s35, 0
	v_mov_b32_e32 v62, v144
	v_mfma_f32_32x32x16_bf16 v[18:33], v[34:37], v[122:125], v[66:81]
	v_mad_i64_i32 v[34:35], s[26:27], v82, s64, 0
	v_mad_i64_i32 v[36:37], s[26:27], v84, s64, 0
	v_readlane_b32 s26, v255, 23
	s_add_u32 s8, s26, s8
	v_readlane_b32 s26, v255, 24
	v_mfma_f32_32x32x16_bf16 v[2:17], v[38:41], v[114:117], v[2:17]
	s_addc_u32 s9, s26, s9
	v_mov_b32_e32 v38, v144
	v_mov_b32_e32 v39, v144
	v_mov_b32_e32 v40, v144
	v_mov_b32_e32 v41, v144
	v_mov_b32_e32 v63, v144
	v_mov_b32_e32 v64, v144
	v_mfma_f32_32x32x16_bf16 v[18:33], v[42:45], v[114:117], v[18:33]
	v_mov_b32_e32 v42, v144
	v_mov_b32_e32 v43, v144
	v_mov_b32_e32 v44, v144
	v_mov_b32_e32 v45, v144
	v_mov_b32_e32 v65, v144
	v_mfma_f32_32x32x16_bf16 v[2:17], v[46:49], v[118:121], v[2:17]
	v_mov_b32_e32 v46, v144
	v_mov_b32_e32 v47, v144
	v_mov_b32_e32 v48, v144
	v_mov_b32_e32 v49, v144
	v_mfma_f32_32x32x16_bf16 v[18:33], v[50:53], v[118:121], v[18:33]
	v_mov_b32_e32 v50, 0
	v_mov_b32_e32 v51, v144
	v_mov_b32_e32 v52, v144
	v_mov_b32_e32 v53, v144
	v_mfma_f32_32x32x16_bf16 v[2:17], v[54:57], v[126:129], v[2:17]
	v_mov_b32_e32 v54, v144
	v_mov_b32_e32 v55, v144
	v_mov_b32_e32 v56, v144
	v_mov_b32_e32 v57, v144
	v_mfma_f32_32x32x16_bf16 v[18:33], v[58:61], v[126:129], v[18:33]
	s_nop 6
	v_exp_f32_e32 v145, v2
	v_exp_f32_e32 v146, v3
	v_exp_f32_e32 v147, v4
	v_exp_f32_e32 v148, v5
	v_exp_f32_e32 v149, v6
	v_exp_f32_e32 v150, v7
	v_exp_f32_e32 v151, v8
	v_exp_f32_e32 v161, v18
	v_exp_f32_e32 v162, v19
	v_exp_f32_e32 v163, v20
	v_exp_f32_e32 v164, v21
	v_exp_f32_e32 v165, v22
	v_exp_f32_e32 v166, v23
	v_exp_f32_e32 v167, v24
	v_exp_f32_e32 v152, v9
	v_exp_f32_e32 v168, v25
	v_exp_f32_e32 v153, v10
	v_exp_f32_e32 v169, v26
	v_exp_f32_e32 v154, v11
	v_exp_f32_e32 v170, v27
	v_exp_f32_e32 v155, v12
	v_exp_f32_e32 v171, v28
	v_exp_f32_e32 v156, v13
	v_exp_f32_e32 v172, v29
	v_exp_f32_e32 v157, v14
	v_exp_f32_e32 v173, v30
	v_exp_f32_e32 v158, v15
	v_exp_f32_e32 v175, v31
	v_exp_f32_e32 v159, v16
	v_exp_f32_e32 v177, v32
	v_exp_f32_e32 v160, v17
	v_exp_f32_e32 v178, v33
	v_bitop3_b32 v2, v83, 7, v176 bitop3:0x48
	v_lshl_or_b32 v34, v2, 4, v34
	v_bitop3_b32 v2, v85, 7, v176 bitop3:0x48
	v_lshl_or_b32 v36, v2, 4, v36
	v_lshl_add_u64 v[134:135], s[8:9], 0, v[34:35]
	v_lshl_add_u64 v[136:137], s[8:9], 0, v[36:37]
	v_mov_b32_e32 v2, 0
	v_mov_b32_e32 v3, v144
	v_mov_b32_e32 v4, v144
	v_mov_b32_e32 v5, v144
	v_mov_b32_e32 v6, v144
	v_mov_b32_e32 v7, v144
	v_mov_b32_e32 v8, v144
	v_mov_b32_e32 v9, v144
	v_mov_b32_e32 v10, v144
	v_mov_b32_e32 v11, v144
	v_mov_b32_e32 v12, v144
	v_mov_b32_e32 v13, v144
	v_mov_b32_e32 v14, v144
	v_mov_b32_e32 v15, v144
	v_mov_b32_e32 v16, v144
	v_mov_b32_e32 v17, v144
	v_mov_b32_e32 v18, 0
	v_mov_b32_e32 v19, v144
	v_mov_b32_e32 v20, v144
	v_mov_b32_e32 v21, v144
	v_mov_b32_e32 v22, v144
	v_mov_b32_e32 v23, v144
	v_mov_b32_e32 v24, v144
	v_mov_b32_e32 v25, v144
	v_mov_b32_e32 v26, v144
	v_mov_b32_e32 v27, v144
	v_mov_b32_e32 v28, v144
	v_mov_b32_e32 v29, v144
	v_mov_b32_e32 v30, v144
	v_mov_b32_e32 v31, v144
	v_mov_b32_e32 v32, v144
	v_mov_b32_e32 v33, v144
	v_mov_b32_e32 v34, 0
	v_mov_b32_e32 v35, v144
	v_mov_b32_e32 v36, v144
	v_mov_b32_e32 v37, v144
	v_mov_b32_e32 v58, v144
	v_mov_b32_e32 v59, v144
	v_mov_b32_e32 v60, v144
	v_mov_b32_e32 v61, v144
	v_and_b32_e32 v225, 31, v176
	v_ashrrev_i32_e32 v228, 5, v176
	v_add_u32_e32 v229, s36, v228
	v_bitop3_b32 v229, v229, v176, 15 bitop3:0x78
	v_lshlrev_b32_e32 v229, 4, v229
	v_lshl_add_u32 v229, v225, 8, v229
	v_lshrrev_b32_e32 v233, 1, v176
	v_bitop3_b32 v228, v233, v228, 7 bitop3:0x6c
	v_lshlrev_b32_e32 v228, 4, v228
	v_lshl_add_u32 v228, v225, 7, v228
	v_add_u32_e32 v228, 0x4000, v228

.LBB0_629:
	s_add_i32 s26, s34, 0xffff0000
	s_and_b32 s26, s26, 0x18000
	v_add_u32_e32 v87, s26, v229
	s_add_i32 s26, s34, 0xfffe8000
	s_and_b32 s26, s26, 0x18000
	v_add_u32_e32 v179, s26, v228
	v_xor_b32_e32 v89, 32, v87
	v_xor_b32_e32 v90, 64, v87
	v_xor_b32_e32 v88, 0x60, v87
	v_xor_b32_e32 v193, 32, v179
	v_xor_b32_e32 v195, 64, v179
	v_xor_b32_e32 v224, 0x60, v179
	ds_read_b128 v[82:85], v87 offset:0
	ds_read_b128 v[184:187], v87 offset:0x2000
	ds_read_b128 v[188:191], v89 offset:0
	ds_read_b128 v[196:199], v89 offset:0x2000
	ds_read_b128 v[200:203], v90 offset:0
	ds_read_b128 v[204:207], v90 offset:0x2000
	ds_read_b128 v[208:211], v88 offset:0
	ds_read_b128 v[212:215], v88 offset:0x2000
	v_cvt_pk_bf16_f32 v216, v145, v146
	v_cvt_pk_bf16_f32 v217, v147, v148
	v_cvt_pk_bf16_f32 v218, v149, v150
	v_cvt_pk_bf16_f32 v219, v151, v152
	v_cvt_pk_bf16_f32 v220, v153, v154
	v_cvt_pk_bf16_f32 v221, v155, v156
	v_cvt_pk_bf16_f32 v222, v157, v158
	v_cvt_pk_bf16_f32 v223, v159, v160
	v_cvt_pk_bf16_f32 v242, v161, v162
	v_cvt_pk_bf16_f32 v243, v163, v164
	v_cvt_pk_bf16_f32 v244, v165, v166
	v_cvt_pk_bf16_f32 v245, v167, v168
	v_cvt_pk_bf16_f32 v246, v169, v170
	v_cvt_pk_bf16_f32 v247, v171, v172
	v_cvt_pk_bf16_f32 v248, v173, v175
	v_cvt_pk_bf16_f32 v249, v177, v178
	s_nop 0
	s_waitcnt lgkmcnt(0)
	s_nop 0
	v_mfma_f32_32x32x16_bf16 v[98:113], v[82:85], v[122:125], v[66:81]
	v_add_f32_e32 v226, v145, v161
	v_add_f32_e32 v226, v226, v146
	v_add_f32_e32 v226, v226, v162
	v_add_f32_e32 v226, v226, v147
	v_mfma_f32_32x32x16_bf16 v[82:97], v[184:187], v[122:125], v[66:81]
	v_add_f32_e32 v226, v226, v163
	v_add_f32_e32 v226, v226, v148
	v_add_f32_e32 v226, v226, v164
	v_add_f32_e32 v226, v226, v149
	v_mfma_f32_32x32x16_bf16 v[98:113], v[188:191], v[114:117], v[98:113]
	v_add_f32_e32 v226, v226, v165
	v_add_f32_e32 v226, v226, v150
	v_add_f32_e32 v226, v226, v166
	v_add_f32_e32 v226, v226, v151
	v_mfma_f32_32x32x16_bf16 v[82:97], v[196:199], v[114:117], v[82:97]
	ds_read_b128 v[184:187], v179 offset:0
	ds_read_b128 v[188:191], v193 offset:0
	ds_read_b128 v[196:199], v195 offset:0
	ds_read_b128 v[180:183], v224 offset:0
	v_add_f32_e32 v226, v226, v167
	v_add_f32_e32 v226, v226, v152
	v_add_f32_e32 v226, v226, v168
	v_add_f32_e32 v226, v226, v153
	v_mfma_f32_32x32x16_bf16 v[98:113], v[200:203], v[118:121], v[98:113]
	v_add_f32_e32 v226, v226, v169
	v_add_f32_e32 v226, v226, v154
	v_add_f32_e32 v226, v226, v170
	v_add_f32_e32 v226, v226, v155
	v_mfma_f32_32x32x16_bf16 v[82:97], v[204:207], v[118:121], v[82:97]
	v_add_f32_e32 v226, v226, v171
	v_add_f32_e32 v226, v226, v156
	v_add_f32_e32 v226, v226, v172
	v_add_f32_e32 v226, v226, v157
	v_mfma_f32_32x32x16_bf16 v[98:113], v[208:211], v[126:129], v[98:113]
	v_add_f32_e32 v226, v226, v173
	v_add_f32_e32 v226, v226, v158
	v_add_f32_e32 v226, v226, v175
	v_add_f32_e32 v226, v226, v159
	v_mfma_f32_32x32x16_bf16 v[82:97], v[212:215], v[126:129], v[82:97]
	v_add_f32_e32 v226, v226, v177
	v_add_f32_e32 v226, v226, v160
	v_add_f32_e32 v226, v226, v178
	v_add_f32_e32 v144, v144, v226
	s_waitcnt lgkmcnt(0)
	ds_read_b128 v[200:203], v179 offset:0x1000
	ds_read_b128 v[204:207], v193 offset:0x1000
	ds_read_b128 v[208:211], v195 offset:0x1000
	ds_read_b128 v[212:215], v224 offset:0x1000
	v_mov_b32_e32 v226, -1
	v_mfma_f32_32x32x16_bf16 v[2:17], v[216:219], v[184:187], v[2:17]
	v_exp_f32_e32 v145, v98
	v_exp_f32_e32 v146, v99
	v_mfma_f32_32x32x16_bf16 v[2:17], v[220:223], v[188:191], v[2:17]
	v_exp_f32_e32 v147, v100
	v_exp_f32_e32 v148, v101
	v_mfma_f32_32x32x16_bf16 v[2:17], v[242:245], v[196:199], v[2:17]
	v_exp_f32_e32 v149, v102
	v_exp_f32_e32 v150, v103
	v_mfma_f32_32x32x16_bf16 v[2:17], v[246:249], v[180:183], v[2:17]
	v_exp_f32_e32 v151, v104
	v_exp_f32_e32 v152, v105
	s_waitcnt lgkmcnt(0)
	ds_read_b128 v[180:183], v179 offset:0x2000
	ds_read_b128 v[184:187], v193 offset:0x2000
	ds_read_b128 v[188:191], v195 offset:0x2000
	ds_read_b128 v[196:199], v224 offset:0x2000
	v_mfma_f32_32x32x16_bf16 v[18:33], v[216:219], v[200:203], v[18:33]
	v_exp_f32_e32 v153, v106
	v_exp_f32_e32 v154, v107
	v_mfma_f32_32x32x16_bf16 v[18:33], v[220:223], v[204:207], v[18:33]
	v_exp_f32_e32 v155, v108
	v_exp_f32_e32 v156, v109
	v_mfma_f32_32x32x16_bf16 v[18:33], v[242:245], v[208:211], v[18:33]
	v_exp_f32_e32 v157, v110
	v_exp_f32_e32 v158, v111
	v_mfma_f32_32x32x16_bf16 v[18:33], v[246:249], v[212:215], v[18:33]
	v_exp_f32_e32 v159, v112
	v_exp_f32_e32 v160, v113
	s_waitcnt lgkmcnt(0)
	ds_read_b128 v[200:203], v179 offset:0x3000
	ds_read_b128 v[204:207], v193 offset:0x3000
	ds_read_b128 v[208:211], v195 offset:0x3000
	ds_read_b128 v[212:215], v224 offset:0x3000
	v_mfma_f32_32x32x16_bf16 v[34:49], v[216:219], v[180:183], v[34:49]
	v_exp_f32_e32 v161, v82
	v_exp_f32_e32 v162, v83
	v_mfma_f32_32x32x16_bf16 v[34:49], v[220:223], v[184:187], v[34:49]
	v_exp_f32_e32 v163, v84
	v_exp_f32_e32 v164, v85
	v_mfma_f32_32x32x16_bf16 v[34:49], v[242:245], v[188:191], v[34:49]
	v_exp_f32_e32 v165, v86
	v_exp_f32_e32 v166, v87
	v_mfma_f32_32x32x16_bf16 v[34:49], v[246:249], v[196:199], v[34:49]
	v_exp_f32_e32 v167, v88
	v_exp_f32_e32 v168, v89
	s_waitcnt lgkmcnt(0)
	v_mfma_f32_32x32x16_bf16 v[50:65], v[216:219], v[200:203], v[50:65]
	v_exp_f32_e32 v169, v90
	v_exp_f32_e32 v170, v91
	v_mfma_f32_32x32x16_bf16 v[50:65], v[220:223], v[204:207], v[50:65]
	v_exp_f32_e32 v171, v92
	v_exp_f32_e32 v172, v93
	v_mfma_f32_32x32x16_bf16 v[50:65], v[242:245], v[208:211], v[50:65]
	v_exp_f32_e32 v173, v94
	v_exp_f32_e32 v175, v95
	v_mfma_f32_32x32x16_bf16 v[50:65], v[246:249], v[212:215], v[50:65]
	v_exp_f32_e32 v177, v96
	v_exp_f32_e32 v178, v97
	s_mov_b64 s[26:27], -1
	s_and_b64 vcc, exec, s[8:9]
	s_cbranch_vccz .Ldfm_w4
	s_waitcnt vmcnt(0)
	s_mov_b64 s[26:27], 0
	s_branch .Ldfm_wd

; #define LAS __attribute__((address_space(3)))
; __device__ __forceinline__ void gla_load_gates(KP Pk, Frame& F, int l, int h, int dir, LAS unsigned char* wl) {
;     LAS float* gw = (LAS float*)(wl + GL_GW); LAS float* gb = (LAS float*)(wl + GL_GB);
;     const float* src = Pk->in[I_GGW] + ((size_t)(l * 2 + dir) * 16) * 256 + h * 32;
; #pragma unroll
;     for (int i = 0; i < 8; ++i) { const int e = F.lane + 64 * i; gw[e] = src[(e >> 5) * 256 + (e & 31)]; }
;     if (F.lane < 32) gb[F.lane] = Pk->in[I_GGB][(l * 2 + dir) * 256 + h * 32 + F.lane];
; }
.LBB0_644:
	v_readlane_b32 s5, v254, 42
	s_or_b32 s5, s4, s5
	s_lshl_b32 s60, s5, 12
	s_lshl_b64 s[8:9], s[60:61], 2
	s_add_u32 s8, s96, s8
	s_addc_u32 s9, s97, s9
	v_lshl_add_u64 v[2:3], v[78:79], 2, s[8:9]
	global_load_dword v212, v[2:3], off
	v_lshl_add_u64 v[2:3], v[80:81], 2, s[8:9]
	global_load_dword v213, v[2:3], off
	v_lshl_add_u64 v[2:3], v[82:83], 2, s[8:9]
	global_load_dword v214, v[2:3], off
	v_lshl_add_u64 v[2:3], v[84:85], 2, s[8:9]
	global_load_dword v215, v[2:3], off
	v_lshl_add_u64 v[2:3], v[86:87], 2, s[8:9]
	global_load_dword v216, v[2:3], off
	v_lshl_add_u64 v[2:3], v[88:89], 2, s[8:9]
	global_load_dword v217, v[2:3], off
	v_lshl_add_u64 v[2:3], v[90:91], 2, s[8:9]
	global_load_dword v218, v[2:3], off
	v_lshl_add_u64 v[2:3], v[92:93], 2, s[8:9]
	global_load_dword v219, v[2:3], off
	s_waitcnt vmcnt(0)
	ds_write2st64_b32 v158, v212, v213 offset0:52 offset1:53
	ds_write2st64_b32 v158, v214, v215 offset0:54 offset1:55
	ds_write2st64_b32 v158, v216, v217 offset0:56 offset1:57
	ds_write2st64_b32 v158, v218, v219 offset0:58 offset1:59
	s_and_saveexec_b64 s[8:9], s[38:39]
	s_cbranch_execz .LBB0_646
	s_load_dwordx2 s[26:27], s[48:49], 0x58
	v_lshl_add_u32 v2, s5, 8, v159
	v_ashrrev_i32_e32 v3, 31, v2
	s_waitcnt lgkmcnt(0)
	v_lshl_add_u64 v[2:3], v[2:3], 2, s[26:27]
	global_load_dword v1, v[2:3], off
	s_waitcnt vmcnt(0)
	ds_write_b32 v158, v1 offset:15360

; __device__ __forceinline__ void gla_pass_b(KP Pk, Frame& F, int l, int b, int h, int c, LAS unsigned char* wl) {
;     ...
;         { const int gsel = cc / GGRP;
; #pragma unroll 1
;           for (int gp = 0; gp <= gsel; ++gp) {
;             const bool fin = gp == gsel;
;             const float* sp = fin ? (const float*)(ws + WS_GSL) + ((size_t)(seq + dir) * NCH + cc) * 2048 : (const float*)(ws + WS_GGS) + ((size_t)(seq + dir) * NGRP + gp) * 2048;
;             const float* apx = fin ? (const float*)(ws + WS_GAE) + ((size_t)(seq + dir) * NCH + cc) * 32 : (const float*)(ws + WS_GGA) + ((size_t)(seq + dir) * NGRP + gp) * 32;
; #pragma unroll
;             for (int db = 0; db < 2; ++db) { const f32x4 av = *(const f32x4*)(apx + 16 * db + 4 * kg);
; #pragma unroll
;                 for (int nb = 0; nb < 4; ++nb)
; #pragma unroll
;                     for (int i = 0; i < 4; ++i) Sr[db][nb][i] = av[i] * Sr[db][nb][i] + sp[(16 * db + 4 * kg + i) * 64 + 16 * nb + r16]; } } }
.LBB0_648:
	s_lshl_b64 s[8:9], s[60:61], 13
	s_add_u32 s37, s84, s8
	s_addc_u32 s40, s90, s9
	s_lshl_b64 s[8:9], s[60:61], 7
	s_add_u32 s41, s86, s8
	s_addc_u32 s45, s59, s9
	s_cmp_eq_u32 s35, 0
	s_cselect_b32 s9, s26, s40
	s_cselect_b32 s8, s5, s37
	s_cselect_b32 s37, s34, s45
	s_cselect_b32 s40, s27, s41
	v_mov_b32_e32 v34, s40
	v_mov_b32_e32 v35, s37
	v_lshl_add_u64 v[38:39], v[62:63], 2, v[34:35]
	s_add_i32 s60, s60, 1
	s_add_i32 s35, s35, 1
	s_cmp_eq_u32 s35, 1
	global_load_dwordx4 v[34:37], v[38:39], off
	global_load_dwordx4 v[208:211], v[38:39], off offset:64
	v_lshl_add_u64 v[40:41], v[64:65], 2, s[8:9]
	global_load_dword v212, v[40:41], off
	v_lshl_add_u64 v[38:39], v[68:69], 2, s[8:9]
	global_load_dword v213, v[38:39], off offset:256
	global_load_dword v214, v[38:39], off offset:512
	global_load_dword v216, v[38:39], off offset:64
	global_load_dword v220, v[38:39], off offset:128
	global_load_dword v224, v[38:39], off offset:192
	v_lshl_add_u64 v[40:41], v[66:67], 2, s[8:9]
	global_load_dword v215, v[40:41], off
	v_lshl_add_u64 v[38:39], v[94:95], 2, s[8:9]
	global_load_dword v217, v[38:39], off offset:256
	global_load_dword v218, v[38:39], off offset:512
	v_lshl_add_u64 v[40:41], v[96:97], 2, s[8:9]
	global_load_dword v219, v[40:41], off offset:64
	global_load_dword v223, v[40:41], off offset:128
	global_load_dword v243, v[40:41], off offset:192
	v_lshl_add_u64 v[38:39], v[98:99], 2, s[8:9]
	global_load_dword v221, v[38:39], off offset:256
	global_load_dword v222, v[38:39], off offset:512
	v_lshl_add_u64 v[40:41], v[100:101], 2, s[8:9]
	global_load_dword v225, v[40:41], off offset:256
	global_load_dword v242, v[40:41], off offset:512
	v_lshl_add_u64 v[38:39], v[106:107], 2, s[8:9]
	global_load_dword v244, v[38:39], off offset:64
	global_load_dword v44, v[38:39], off offset:128
	global_load_dword v42, v[38:39], off offset:192
	v_lshl_add_u64 v[40:41], v[108:109], 2, s[8:9]
	global_load_dword v245, v[40:41], off offset:64
	global_load_dword v45, v[40:41], off offset:128
	global_load_dword v43, v[40:41], off offset:192
	v_lshl_add_u64 v[38:39], v[70:71], 2, s[8:9]
	global_load_dword v246, v[38:39], off
	v_lshl_add_u64 v[40:41], v[72:73], 2, s[8:9]
	global_load_dword v247, v[40:41], off
	v_lshl_add_u64 v[38:39], v[74:75], 2, s[8:9]
	global_load_dword v248, v[38:39], off
	v_lshl_add_u64 v[40:41], v[76:77], 2, s[8:9]
	global_load_dword v249, v[40:41], off
	v_lshl_add_u64 v[38:39], v[102:103], 2, s[8:9]
	global_load_dword v250, v[38:39], off offset:64
	global_load_dword v228, v[38:39], off offset:128
	global_load_dword v46, v[38:39], off offset:192
	v_lshl_add_u64 v[40:41], v[104:105], 2, s[8:9]
	global_load_dword v251, v[40:41], off offset:64
	global_load_dword v229, v[40:41], off offset:128
	global_load_dword v47, v[40:41], off offset:192
	s_waitcnt vmcnt(0)
	v_pk_fma_f32 v[30:31], v[30:31], v[34:35], v[212:213]
	v_pk_fma_f32 v[32:33], v[32:33], v[36:37], v[214:215]
	v_pk_fma_f32 v[26:27], v[26:27], v[34:35], v[216:217]
	v_pk_fma_f32 v[28:29], v[28:29], v[36:37], v[218:219]
	v_pk_fma_f32 v[22:23], v[22:23], v[34:35], v[220:221]
	v_pk_fma_f32 v[24:25], v[24:25], v[36:37], v[222:223]
	v_pk_fma_f32 v[14:15], v[14:15], v[34:35], v[224:225]
	v_pk_fma_f32 v[16:17], v[16:17], v[36:37], v[242:243]
	v_pk_fma_f32 v[12:13], v[12:13], v[210:211], v[244:245]
	v_pk_fma_f32 v[18:19], v[18:19], v[208:209], v[246:247]
	v_pk_fma_f32 v[20:21], v[20:21], v[210:211], v[248:249]
	v_pk_fma_f32 v[10:11], v[10:11], v[208:209], v[250:251]
	v_pk_fma_f32 v[6:7], v[6:7], v[208:209], v[228:229]
	v_pk_fma_f32 v[8:9], v[8:9], v[210:211], v[44:45]
	v_pk_fma_f32 v[2:3], v[2:3], v[208:209], v[46:47]
	v_pk_fma_f32 v[4:5], v[4:5], v[210:211], v[42:43]
	s_cbranch_scc0 .LBB0_648
	s_branch .LBB0_650
